# hoist qa gather before compute in output waves; single vmcnt(0) before outputs
# speedup vs baseline: 1.0129x; 1.0129x over previous
.LBB0_93:
	s_or_b64 exec, exec, s[6:7]
	s_waitcnt lgkmcnt(0)
	ds_read_b128 v[194:197], v179
	ds_read_b128 v[198:201], v179 offset:32
	ds_read_b128 v[202:205], v179 offset:64
	v_add_u32_e32 v66, 0x20c40, v188
	ds_read_b32 v191, v66
	v_add_u32_e32 v66, 0x20c00, v188
	s_waitcnt lgkmcnt(3)
	v_mfma_f32_32x32x16_f16 v[68:83], v[98:101], v[194:197], v[2:17]
	ds_read_b32 v192, v66
	ds_read_b128 v[206:209], v179 offset:96
	s_and_b32 s0, s17, 1
	s_waitcnt lgkmcnt(2)
	v_lshlrev_b32_e32 v66, 4, v191
	v_and_or_b32 v66, v66, s28, v1
	v_lshlrev_b32_e32 v66, 4, v66
	global_load_dwordx4 v[162:165], v66, s[22:23]
	s_mulk_i32 s0, 0x1200
	v_mfma_f32_32x32x16_f16 v[68:83], v[102:105], v[198:201], v[68:83]
	v_mfma_f32_32x32x16_f16 v[68:83], v[106:109], v[202:205], v[68:83]
	s_waitcnt lgkmcnt(0)
	v_mfma_f32_32x32x16_f16 v[68:83], v[110:113], v[206:209], v[68:83]
	v_lshlrev_b32_e32 v66, 4, v192
	v_and_or_b32 v66, v66, s28, v1
	v_lshlrev_b32_e32 v66, 4, v66
	global_load_dwordx4 v[216:219], v66, s[22:23]
	s_nop 7
	v_and_b32_e32 v84, 0xffffffc0, v68
	v_and_or_b32 v85, v69, s16, 1
	v_and_or_b32 v86, v70, s16, 2
	v_and_or_b32 v87, v71, s16, 3
	v_and_or_b32 v88, v72, s16, 4
	v_and_or_b32 v89, v73, s16, 5
	v_and_or_b32 v90, v74, s16, 6
	v_and_or_b32 v91, v75, s16, 7
	v_and_or_b32 v92, v76, s16, 8
	v_and_or_b32 v93, v77, s16, 9
	v_and_or_b32 v94, v78, s16, 10
	v_and_or_b32 v95, v79, s16, 11
	v_and_or_b32 v96, v80, s16, 12
	v_and_or_b32 v97, v81, s16, 13
	v_mfma_f32_32x32x16_f16 v[66:81], v[114:117], v[194:197], v[18:33]
	v_med3_f32 v193, v84, v85, s25
	v_min3_f32 v84, v84, s25, v85
	v_med3_f32 v85, v84, v86, v87
	v_min3_f32 v84, v84, v86, v87
	v_med3_f32 v86, v84, v88, v89
	v_min3_f32 v84, v84, v88, v89
	v_min3_f32 v85, v193, s25, v85
	v_mfma_f32_32x32x16_f16 v[66:81], v[118:121], v[198:201], v[66:81]
	v_med3_f32 v87, v84, v90, v91
	v_min3_f32 v84, v84, v90, v91
	v_min3_f32 v85, v85, v86, v87
	v_med3_f32 v86, v84, v92, v93
	v_min3_f32 v84, v84, v92, v93
	v_med3_f32 v87, v84, v94, v95
	v_min3_f32 v84, v84, v94, v95
	v_mfma_f32_32x32x16_f16 v[66:81], v[122:125], v[202:205], v[66:81]
	v_and_or_b32 v82, v82, s16, 14
	v_and_or_b32 v83, v83, s16, 15
	v_min3_f32 v85, v85, v86, v87
	v_med3_f32 v86, v84, v96, v97
	v_min3_f32 v84, v84, v96, v97
	v_med3_f32 v87, v84, v82, v83
	v_min3_f32 v193, v84, v82, v83
	v_mfma_f32_32x32x16_f16 v[66:81], v[126:129], v[206:209], v[66:81]
	v_min3_f32 v210, v85, v86, v87
	v_mfma_f32_32x32x16_f16 v[82:97], v[130:133], v[194:197], v[34:49]
	s_nop 9
	v_and_or_b32 v66, v66, s16, 16
	v_and_or_b32 v67, v67, s16, 17
	v_and_or_b32 v68, v68, s16, 18
	v_and_or_b32 v69, v69, s16, 19
	v_med3_f32 v211, v193, v66, v67
	v_min3_f32 v66, v193, v66, v67
	v_and_or_b32 v70, v70, s16, 20
	v_and_or_b32 v71, v71, s16, 21
	v_med3_f32 v67, v66, v68, v69
	v_min3_f32 v66, v66, v68, v69
	v_and_or_b32 v72, v72, s16, 22
	v_and_or_b32 v73, v73, s16, 23
	v_med3_f32 v68, v66, v70, v71
	v_min3_f32 v66, v66, v70, v71
	v_and_or_b32 v74, v74, s16, 24
	v_and_or_b32 v75, v75, s16, 25
	v_min3_f32 v67, v210, v211, v67
	v_med3_f32 v69, v66, v72, v73
	v_min3_f32 v66, v66, v72, v73
	v_and_or_b32 v76, v76, s16, 26
	v_and_or_b32 v77, v77, s16, 27
	v_min3_f32 v67, v67, v68, v69
	v_med3_f32 v68, v66, v74, v75
	v_min3_f32 v66, v66, v74, v75
	v_and_or_b32 v78, v78, s16, 28
	v_and_or_b32 v79, v79, s16, 29
	v_med3_f32 v69, v66, v76, v77
	v_min3_f32 v66, v66, v76, v77
	v_and_or_b32 v80, v80, s16, 30
	v_and_or_b32 v81, v81, s16, 31
	v_min3_f32 v67, v67, v68, v69
	v_med3_f32 v68, v66, v78, v79
	v_min3_f32 v66, v66, v78, v79
	v_med3_f32 v69, v66, v80, v81
	v_mfma_f32_32x32x16_f16 v[82:97], v[134:137], v[198:201], v[82:97]
	v_min3_f32 v193, v66, v80, v81
	v_min3_f32 v210, v67, v68, v69
	v_mfma_f32_32x32x16_f16 v[66:81], v[146:149], v[194:197], v[50:65]
	v_mfma_f32_32x32x16_f16 v[82:97], v[138:141], v[202:205], v[82:97]
	v_mfma_f32_32x32x16_f16 v[66:81], v[150:153], v[198:201], v[66:81]
	v_mfma_f32_32x32x16_f16 v[82:97], v[142:145], v[206:209], v[82:97]
	v_mfma_f32_32x32x16_f16 v[66:81], v[154:157], v[202:205], v[66:81]
	s_nop 10
	v_and_or_b32 v82, v82, s16, 32
	v_and_or_b32 v83, v83, s16, 33
	v_and_or_b32 v84, v84, s16, 34
	v_and_or_b32 v85, v85, s16, 35
	v_med3_f32 v194, v193, v82, v83
	v_min3_f32 v82, v193, v82, v83
	v_and_or_b32 v86, v86, s16, 36
	v_mfma_f32_32x32x16_f16 v[66:81], v[158:161], v[206:209], v[66:81]
	v_and_or_b32 v87, v87, s16, 37
	v_med3_f32 v83, v82, v84, v85
	v_min3_f32 v82, v82, v84, v85
	v_and_or_b32 v88, v88, s16, 38
	v_and_or_b32 v89, v89, s16, 39
	v_med3_f32 v84, v82, v86, v87
	v_min3_f32 v82, v82, v86, v87
	v_and_or_b32 v90, v90, s16, 40
	v_and_or_b32 v91, v91, s16, 41
	v_min3_f32 v83, v210, v194, v83
	v_med3_f32 v85, v82, v88, v89
	v_min3_f32 v82, v82, v88, v89
	v_and_or_b32 v92, v92, s16, 42
	v_and_or_b32 v93, v93, s16, 43
	v_min3_f32 v83, v83, v84, v85
	v_med3_f32 v84, v82, v90, v91
	v_min3_f32 v82, v82, v90, v91
	v_and_or_b32 v94, v94, s16, 44
	v_and_or_b32 v95, v95, s16, 45
	v_med3_f32 v85, v82, v92, v93
	v_min3_f32 v82, v82, v92, v93
	v_and_or_b32 v96, v96, s16, 46
	v_and_or_b32 v97, v97, s16, 47
	v_min3_f32 v83, v83, v84, v85
	v_med3_f32 v84, v82, v94, v95
	v_min3_f32 v82, v82, v94, v95
	v_med3_f32 v85, v82, v96, v97
	v_min3_f32 v82, v82, v96, v97
	v_and_or_b32 v66, v66, s16, 48
	v_and_or_b32 v67, v67, s16, 49
	v_min3_f32 v83, v83, v84, v85
	v_and_or_b32 v68, v68, s16, 50
	v_and_or_b32 v69, v69, s16, 51
	v_med3_f32 v84, v82, v66, v67
	v_min3_f32 v66, v82, v66, v67
	v_and_or_b32 v70, v70, s16, 52
	v_and_or_b32 v71, v71, s16, 53
	v_med3_f32 v67, v66, v68, v69
	v_min3_f32 v66, v66, v68, v69
	v_and_or_b32 v72, v72, s16, 54
	v_and_or_b32 v73, v73, s16, 55
	v_med3_f32 v68, v66, v70, v71
	v_min3_f32 v66, v66, v70, v71
	v_and_or_b32 v74, v74, s16, 56
	v_and_or_b32 v75, v75, s16, 57
	v_min3_f32 v67, v83, v84, v67
	v_med3_f32 v69, v66, v72, v73
	v_min3_f32 v66, v66, v72, v73
	v_and_or_b32 v76, v76, s16, 58
	v_and_or_b32 v77, v77, s16, 59
	v_min3_f32 v67, v67, v68, v69
	v_med3_f32 v68, v66, v74, v75
	v_min3_f32 v66, v66, v74, v75
	v_and_or_b32 v78, v78, s16, 60
	v_and_or_b32 v79, v79, s16, 61
	v_med3_f32 v69, v66, v76, v77
	v_min3_f32 v66, v66, v76, v77
	v_and_or_b32 v80, v80, s16, 62
	v_or_b32_e32 v81, 63, v81
	v_min3_f32 v67, v67, v68, v69
	v_med3_f32 v68, v66, v78, v79
	v_min3_f32 v66, v66, v78, v79
	v_med3_f32 v69, v66, v80, v81
	v_min3_f32 v66, v66, v80, v81
	v_min3_f32 v67, v67, v68, v69
	v_add_u32_e32 v68, s0, v177
	v_cmp_lt_i32_e64 s[0:1], -1, v192
	ds_write_b64 v68, v[66:67]
	s_waitcnt vmcnt(0)
	s_and_saveexec_b64 s[6:7], s[0:1]
	s_cbranch_execz .LBB0_95
	s_and_b32 s0, s29, 3
	v_lshl_add_u32 v70, s0, 13, v175
	ds_read_b128 v[70:73], v70
	s_waitcnt lgkmcnt(0)
	v_pk_add_f32 v[66:67], v[216:217], v[70:71] neg_lo:[0,1] neg_hi:[0,1]
	v_pk_add_f32 v[74:75], v[218:219], v[72:73] neg_lo:[0,1] neg_hi:[0,1]
	v_pk_mul_f32 v[76:77], v[66:67], v[66:67]
	v_pk_add_f32 v[66:67], v[70:71], v[66:67]
	v_pk_add_f32 v[68:69], v[72:73], v[74:75]
	v_pk_mul_f32 v[70:71], v[74:75], v[74:75]
	global_store_dwordx4 v[168:169], v[66:69], off nt
	s_nop 1
	v_add_f32_e32 v66, v76, v77
	v_add_f32_e32 v66, v66, v70
	v_add_f32_e32 v66, v66, v71
	v_add_f32_e32 v167, v167, v66
.LBB0_95:
	s_or_b64 exec, exec, s[6:7]
	v_cmp_lt_i32_e64 s[0:1], -1, v191
	s_and_saveexec_b64 s[6:7], s[0:1]
	s_cbranch_execz .LBB0_87
	s_and_b32 s0, s29, 3
	v_lshl_add_u32 v66, s0, 13, v174
	ds_read_b128 v[66:69], v66
	s_waitcnt lgkmcnt(0)
	v_pk_add_f32 v[70:71], v[162:163], v[66:67] neg_lo:[0,1] neg_hi:[0,1]
	v_pk_add_f32 v[72:73], v[164:165], v[68:69] neg_lo:[0,1] neg_hi:[0,1]
	v_pk_mul_f32 v[74:75], v[70:71], v[70:71]
	v_pk_add_f32 v[66:67], v[66:67], v[70:71]
	v_pk_add_f32 v[68:69], v[68:69], v[72:73]
	v_pk_mul_f32 v[70:71], v[72:73], v[72:73]
	global_store_dwordx4 v[170:171], v[66:69], off nt
	s_nop 1
	v_add_f32_e32 v66, v74, v75
	v_add_f32_e32 v66, v66, v70
	v_add_f32_e32 v66, v66, v71
	v_add_f32_e32 v167, v167, v66
	s_branch .LBB0_87
